# NA main loop: first V fragments for P.V read before the exp block into dead bias registers; head of the row-sum add chain split in two
# baseline (speedup 1.0000x reference)
.LBB0_601:
	v_add_u32_e32 v239, s1, v182
	ds_read_b64_tr_b16 v[206:207], v239 offset:0
	ds_read_b64_tr_b16 v[208:209], v239 offset:0x800
	ds_read_b64_tr_b16 v[210:211], v239 offset:0x1000
	ds_read_b64_tr_b16 v[212:213], v239 offset:0x1800
	ds_read_b64_tr_b16 v[214:215], v239 offset:0x2000
	ds_read_b64_tr_b16 v[216:217], v239 offset:0x2800
	ds_read_b64_tr_b16 v[218:219], v239 offset:0x3000
	ds_read_b64_tr_b16 v[220:221], v239 offset:0x3800
	v_cndmask_b32_e64 v184, v98, v184, s[72:73]
	v_mul_f32_e32 v98, 0xbe0293ee, v184
	v_fmamk_f32 v82, v82, 0x3e0293ee, v98
	v_fmamk_f32 v83, v83, 0x3e0293ee, v98
	v_fmamk_f32 v84, v84, 0x3e0293ee, v98
	v_fmamk_f32 v85, v85, 0x3e0293ee, v98
	v_fmamk_f32 v86, v86, 0x3e0293ee, v98
	v_fmamk_f32 v87, v87, 0x3e0293ee, v98
	v_fmamk_f32 v88, v88, 0x3e0293ee, v98
	v_fmamk_f32 v89, v89, 0x3e0293ee, v98
	v_fmamk_f32 v90, v90, 0x3e0293ee, v98
	v_fmamk_f32 v91, v91, 0x3e0293ee, v98
	v_fmamk_f32 v92, v92, 0x3e0293ee, v98
	v_fmamk_f32 v93, v93, 0x3e0293ee, v98
	v_fmamk_f32 v94, v94, 0x3e0293ee, v98
	v_fmamk_f32 v95, v95, 0x3e0293ee, v98
	v_fmamk_f32 v96, v96, 0x3e0293ee, v98
	v_fmamk_f32 v97, v97, 0x3e0293ee, v98
	v_fmamk_f32 v0, v0, 0x3e0293ee, v98
	v_fmamk_f32 v66, v66, 0x3e0293ee, v98
	v_fmamk_f32 v67, v67, 0x3e0293ee, v98
	v_fmamk_f32 v68, v68, 0x3e0293ee, v98
	v_fmamk_f32 v69, v69, 0x3e0293ee, v98
	v_fmamk_f32 v70, v70, 0x3e0293ee, v98
	v_fmamk_f32 v71, v71, 0x3e0293ee, v98
	v_fmamk_f32 v72, v72, 0x3e0293ee, v98
	v_fmamk_f32 v73, v73, 0x3e0293ee, v98
	v_fmamk_f32 v74, v74, 0x3e0293ee, v98
	v_fmamk_f32 v75, v75, 0x3e0293ee, v98
	v_fmamk_f32 v76, v76, 0x3e0293ee, v98
	v_fmamk_f32 v77, v77, 0x3e0293ee, v98
	v_fmamk_f32 v78, v78, 0x3e0293ee, v98
	v_fmamk_f32 v79, v79, 0x3e0293ee, v98
	v_fmac_f32_e32 v98, 0x3e0293ee, v80
	v_exp_f32_e32 v80, v82
	v_exp_f32_e32 v82, v83
	v_exp_f32_e32 v83, v84
	v_exp_f32_e32 v84, v85
	v_exp_f32_e32 v85, v86
	v_exp_f32_e32 v86, v87
	v_exp_f32_e32 v87, v88
	v_exp_f32_e32 v88, v89
	v_exp_f32_e32 v89, v90
	v_exp_f32_e32 v90, v91
	v_exp_f32_e32 v91, v92
	v_exp_f32_e32 v92, v93
	v_exp_f32_e32 v93, v94
	v_exp_f32_e32 v94, v95
	v_exp_f32_e32 v95, v96
	v_exp_f32_e32 v96, v97
	v_exp_f32_e32 v97, v0
	v_add_f32_e32 v0, v80, v82
	v_add_f32_e32 v222, v83, v84
	v_add_f32_e32 v0, v85, v0
	v_add_f32_e32 v222, v86, v222
	v_add_f32_e32 v0, v87, v0
	v_add_f32_e32 v222, v88, v222
	v_add_f32_e32 v0, v89, v0
	v_add_f32_e32 v222, v90, v222
	v_add_f32_e32 v0, v91, v0
	v_add_f32_e32 v222, v92, v222
	v_add_f32_e32 v0, v93, v0
	v_add_f32_e32 v0, v222, v0
	v_exp_f32_e32 v99, v66
	v_add_f32_e32 v0, v94, v0
	v_exp_f32_e32 v100, v67
	v_add_f32_e32 v0, v95, v0
	v_exp_f32_e32 v101, v68
	v_add_f32_e32 v0, v96, v0
	v_exp_f32_e32 v102, v69
	v_add_f32_e32 v0, v97, v0
	v_exp_f32_e32 v103, v70
	v_add_f32_e32 v0, v99, v0
	v_exp_f32_e32 v104, v71
	v_add_f32_e32 v0, v100, v0
	v_exp_f32_e32 v105, v72
	v_add_f32_e32 v0, v101, v0
	v_exp_f32_e32 v106, v73
	v_add_f32_e32 v0, v102, v0
	v_exp_f32_e32 v107, v74
	v_add_f32_e32 v0, v103, v0
	v_exp_f32_e32 v108, v75
	v_add_f32_e32 v0, v104, v0
	v_exp_f32_e32 v109, v76
	v_add_f32_e32 v0, v105, v0
	v_exp_f32_e32 v110, v77
	v_add_f32_e32 v0, v106, v0
	v_exp_f32_e32 v111, v78
	v_add_f32_e32 v0, v107, v0
	v_exp_f32_e32 v112, v79
	v_add_f32_e32 v0, v108, v0
	v_exp_f32_e32 v98, v98
	v_add_f32_e32 v0, v109, v0
	v_add_f32_e32 v0, v110, v0
	v_add_f32_e32 v0, v111, v0
	v_add_f32_e32 v0, v112, v0
	v_add_f32_e32 v0, v98, v0
	v_mov_b32_e32 v66, v0
	s_nop 1
	v_permlane32_swap_b32_e32 v0, v66
	v_add_f32_e32 v0, v0, v66
	v_fmac_f32_e32 v0, v200, v81
	v_cvt_pk_bf16_f32 v66, v80, v82
	v_cvt_pk_bf16_f32 v67, v83, v84
	v_cvt_pk_bf16_f32 v68, v85, v86
	v_cvt_pk_bf16_f32 v69, v87, v88
	v_cvt_pk_bf16_f32 v70, v89, v90
	v_cvt_pk_bf16_f32 v71, v91, v92
	v_cvt_pk_bf16_f32 v72, v93, v94
	v_cvt_pk_bf16_f32 v73, v95, v96
	v_cvt_pk_bf16_f32 v74, v97, v99
	v_cvt_pk_bf16_f32 v75, v100, v101
	v_cvt_pk_bf16_f32 v76, v102, v103
	v_cvt_pk_bf16_f32 v77, v104, v105
	v_cvt_pk_bf16_f32 v78, v106, v107
	v_cvt_pk_bf16_f32 v79, v108, v109
	v_cvt_pk_bf16_f32 v80, v110, v111
	v_cvt_pk_bf16_f32 v81, v112, v98
	s_nop 0
	v_permlane32_swap_b32_e32 v66, v68
	v_permlane32_swap_b32_e32 v67, v69
	v_permlane32_swap_b32_e32 v70, v72
	v_permlane32_swap_b32_e32 v71, v73
	v_permlane32_swap_b32_e32 v74, v76
	v_permlane32_swap_b32_e32 v75, v77
	v_permlane32_swap_b32_e32 v78, v80
	v_permlane32_swap_b32_e32 v79, v81
	v_add_u32_e32 v98, s1, v182
	s_waitcnt lgkmcnt(0)
	s_nop 0
	v_mfma_f32_32x32x16_bf16 v[50:65], v[66:69], v[206:209], v[50:65]
	ds_read_b64_tr_b16 v[82:83], v98 offset:0x200
	ds_read_b64_tr_b16 v[84:85], v98 offset:0xa00
	v_mfma_f32_32x32x16_bf16 v[50:65], v[70:73], v[210:213], v[50:65]
	ds_read_b64_tr_b16 v[86:87], v98 offset:0x1200
	ds_read_b64_tr_b16 v[88:89], v98 offset:0x1a00
	v_mfma_f32_32x32x16_bf16 v[50:65], v[74:77], v[214:217], v[50:65]
	ds_read_b64_tr_b16 v[90:91], v98 offset:0x2200
	ds_read_b64_tr_b16 v[92:93], v98 offset:0x2a00
	v_mfma_f32_32x32x16_bf16 v[50:65], v[78:81], v[218:221], v[50:65]
	ds_read_b64_tr_b16 v[94:95], v98 offset:0x3200
	ds_read_b64_tr_b16 v[96:97], v98 offset:0x3a00
	s_waitcnt lgkmcnt(0)
	v_mfma_f32_32x32x16_bf16 v[34:49], v[66:69], v[82:85], v[34:49]
	ds_read_b64_tr_b16 v[82:83], v98 offset:0x400
	ds_read_b64_tr_b16 v[84:85], v98 offset:0xc00
	v_mfma_f32_32x32x16_bf16 v[34:49], v[70:73], v[86:89], v[34:49]
	ds_read_b64_tr_b16 v[86:87], v98 offset:0x1400
	ds_read_b64_tr_b16 v[88:89], v98 offset:0x1c00
	v_mfma_f32_32x32x16_bf16 v[34:49], v[74:77], v[90:93], v[34:49]
	ds_read_b64_tr_b16 v[90:91], v98 offset:0x2400
	ds_read_b64_tr_b16 v[92:93], v98 offset:0x2c00
	v_mfma_f32_32x32x16_bf16 v[34:49], v[78:81], v[94:97], v[34:49]
	ds_read_b64_tr_b16 v[94:95], v98 offset:0x3400
	ds_read_b64_tr_b16 v[96:97], v98 offset:0x3c00
	s_waitcnt lgkmcnt(0)
	v_mfma_f32_32x32x16_bf16 v[18:33], v[66:69], v[82:85], v[18:33]
	ds_read_b64_tr_b16 v[82:83], v98 offset:0x600
	ds_read_b64_tr_b16 v[84:85], v98 offset:0xe00
	v_mfma_f32_32x32x16_bf16 v[18:33], v[70:73], v[86:89], v[18:33]
	ds_read_b64_tr_b16 v[86:87], v98 offset:0x1600
	ds_read_b64_tr_b16 v[88:89], v98 offset:0x1e00
	v_mfma_f32_32x32x16_bf16 v[18:33], v[74:77], v[90:93], v[18:33]
	ds_read_b64_tr_b16 v[90:91], v98 offset:0x2600
	ds_read_b64_tr_b16 v[92:93], v98 offset:0x2e00
	v_mfma_f32_32x32x16_bf16 v[18:33], v[78:81], v[94:97], v[18:33]
	ds_read_b64_tr_b16 v[94:95], v98 offset:0x3600
	ds_read_b64_tr_b16 v[96:97], v98 offset:0x3e00
	s_waitcnt lgkmcnt(0)
	v_mfma_f32_32x32x16_bf16 v[2:17], v[66:69], v[82:85], v[2:17]
	s_waitcnt vmcnt(3)
	v_cvt_f32_fp8_e32 v66, v164
	v_cvt_f32_fp8_sdwa v67, v164 src0_sel:BYTE_1
	s_waitcnt vmcnt(0)
	v_cvt_pk_bf16_f32 v66, v66, v67
	v_cvt_f32_fp8_sdwa v67, v164 src0_sel:BYTE_2
	v_cvt_f32_fp8_sdwa v68, v164 src0_sel:BYTE_3
	v_cvt_pk_bf16_f32 v67, v67, v68
	v_mfma_f32_32x32x16_bf16 v[2:17], v[70:73], v[86:89], v[2:17]
	v_cvt_f32_fp8_e32 v68, v165
	v_cvt_f32_fp8_sdwa v69, v165 src0_sel:BYTE_1
	v_cvt_pk_bf16_f32 v68, v68, v69
	v_cvt_f32_fp8_sdwa v69, v165 src0_sel:BYTE_2
	v_cvt_f32_fp8_sdwa v70, v165 src0_sel:BYTE_3
	v_cvt_pk_bf16_f32 v69, v69, v70
	s_waitcnt vmcnt(2)
	v_cvt_f32_fp8_e32 v70, v162
	v_mfma_f32_32x32x16_bf16 v[2:17], v[74:77], v[90:93], v[2:17]
	v_cvt_f32_fp8_sdwa v71, v162 src0_sel:BYTE_1
	v_cvt_pk_bf16_f32 v70, v70, v71
	v_cvt_f32_fp8_sdwa v71, v162 src0_sel:BYTE_2
	v_cvt_f32_fp8_sdwa v72, v162 src0_sel:BYTE_3
	v_cvt_pk_bf16_f32 v71, v71, v72
	v_cvt_f32_fp8_e32 v72, v163
	v_cvt_f32_fp8_sdwa v73, v163 src0_sel:BYTE_1
	v_cvt_pk_bf16_f32 v72, v72, v73
	v_cvt_f32_fp8_sdwa v73, v163 src0_sel:BYTE_2
	v_cvt_f32_fp8_sdwa v74, v163 src0_sel:BYTE_3
	v_cvt_pk_bf16_f32 v73, v73, v74
	s_waitcnt vmcnt(1)
	v_mfma_f32_32x32x16_bf16 v[2:17], v[78:81], v[94:97], v[2:17]
	s_waitcnt vmcnt(0)
	v_cvt_f32_fp8_e32 v82, v160
	v_cvt_f32_fp8_sdwa v74, v160 src0_sel:BYTE_1
	v_cvt_f32_fp8_sdwa v83, v160 src0_sel:BYTE_2
	v_cvt_f32_fp8_sdwa v75, v160 src0_sel:BYTE_3
	v_mul_f32_e32 v86, v74, v74
	v_mul_f32_e32 v87, v75, v75
	v_cvt_f32_fp8_e32 v84, v161
	v_cvt_f32_fp8_sdwa v76, v161 src0_sel:BYTE_1
	v_fmac_f32_e32 v86, v82, v82
	v_fmac_f32_e32 v87, v83, v83
	v_add_f32_e32 v86, v86, v87
	v_mul_f32_e32 v87, v76, v76
	v_cvt_f32_fp8_sdwa v85, v161 src0_sel:BYTE_2
	v_cvt_f32_fp8_sdwa v77, v161 src0_sel:BYTE_3
	v_fmac_f32_e32 v87, v84, v84
	v_add_f32_e32 v86, v86, v87
	v_mul_f32_e32 v87, v77, v77
	v_fmac_f32_e32 v87, v85, v85
	v_add_f32_e32 v86, v86, v87
	s_nop 1
	s_xor_b32 s1, s1, 0x4000
	s_add_i32 s1, s1, 0
	s_add_i32 s92, s92, 1
	s_addk_i32 s3, 0x4000
	v_add_f32_dpp v86, v86, v86 quad_perm:[1,0,3,2] row_mask:0xf bank_mask:0xf
	s_nop 1
	s_add_u32 s96, s96, 0x2000
	s_addc_u32 s97, s97, 0
	s_cmp_eq_u32 s96, 0x16000
	v_add_f32_dpp v86, v86, v86 quad_perm:[2,3,0,1] row_mask:0xf bank_mask:0xf
	s_nop 1
	v_add_f32_dpp v86, v86, v86 row_half_mirror row_mask:0xf bank_mask:0xf
	s_nop 1
	s_waitcnt lgkmcnt(0)
	v_add_f32_dpp v86, v86, v86 row_mirror row_mask:0xf bank_mask:0xf
	v_fmamk_f32 v86, v86, 0x3c000000, v167
	v_rsq_f32_e32 v86, v86
	s_nop 0
	v_mul_f32_e32 v82, v86, v82
	v_mul_f32_e32 v74, v86, v74
	v_mul_f32_e32 v82, v150, v82
	v_mul_f32_e32 v74, v151, v74
	v_cvt_pk_bf16_f32 v74, v82, v74
	v_mul_f32_e32 v82, v86, v83
	v_mul_f32_e32 v75, v86, v75
	v_mul_f32_e32 v82, v152, v82
	v_mul_f32_e32 v75, v153, v75
	v_cvt_pk_bf16_f32 v75, v82, v75
	v_mul_f32_e32 v82, v86, v84
	v_mul_f32_e32 v76, v86, v76
	v_mul_f32_e32 v82, v146, v82
	v_mul_f32_e32 v76, v147, v76
	v_cvt_pk_bf16_f32 v76, v82, v76
	v_mul_f32_e32 v82, v86, v85
	v_mul_f32_e32 v77, v86, v77
	v_mul_f32_e32 v82, v148, v82
	v_mul_f32_e32 v77, v149, v77
	v_cvt_pk_bf16_f32 v77, v82, v77
	v_cvt_f32_fp8_e32 v82, v158
	v_cvt_f32_fp8_sdwa v78, v158 src0_sel:BYTE_1
	v_cvt_f32_fp8_sdwa v83, v158 src0_sel:BYTE_2
	v_cvt_f32_fp8_sdwa v79, v158 src0_sel:BYTE_3
	v_mul_f32_e32 v86, v78, v78
	v_mul_f32_e32 v87, v79, v79
	v_cvt_f32_fp8_e32 v84, v159
	v_cvt_f32_fp8_sdwa v80, v159 src0_sel:BYTE_1
	v_fmac_f32_e32 v86, v82, v82
	v_fmac_f32_e32 v87, v83, v83
	v_add_f32_e32 v86, v86, v87
	v_mul_f32_e32 v87, v80, v80
	v_cvt_f32_fp8_sdwa v85, v159 src0_sel:BYTE_2
	v_cvt_f32_fp8_sdwa v81, v159 src0_sel:BYTE_3
	v_fmac_f32_e32 v87, v84, v84
	v_add_f32_e32 v86, v86, v87
	v_mul_f32_e32 v87, v81, v81
	v_fmac_f32_e32 v87, v85, v85
	v_add_f32_e32 v86, v86, v87
	s_nop 1
	v_add_f32_dpp v86, v86, v86 quad_perm:[1,0,3,2] row_mask:0xf bank_mask:0xf
	s_nop 1
	v_add_f32_dpp v86, v86, v86 quad_perm:[2,3,0,1] row_mask:0xf bank_mask:0xf
	s_nop 1
	v_add_f32_dpp v86, v86, v86 row_half_mirror row_mask:0xf bank_mask:0xf
	s_nop 1
	s_waitcnt lgkmcnt(0)
	v_add_f32_dpp v86, v86, v86 row_mirror row_mask:0xf bank_mask:0xf
	v_fmamk_f32 v86, v86, 0x3c000000, v167
	v_rsq_f32_e32 v86, v86
	s_nop 0
	v_mul_f32_e32 v82, v86, v82
	v_mul_f32_e32 v78, v86, v78
	v_mul_f32_e32 v82, v150, v82
	v_mul_f32_e32 v78, v151, v78
	v_cvt_pk_bf16_f32 v78, v82, v78
	v_mul_f32_e32 v82, v86, v83
	v_mul_f32_e32 v79, v86, v79
	v_mul_f32_e32 v82, v152, v82
	v_mul_f32_e32 v79, v153, v79
	v_cvt_pk_bf16_f32 v79, v82, v79
	v_mul_f32_e32 v82, v86, v84
	v_mul_f32_e32 v80, v86, v80
	v_mul_f32_e32 v82, v146, v82
	v_mul_f32_e32 v80, v147, v80
	v_cvt_pk_bf16_f32 v80, v82, v80
	v_mul_f32_e32 v82, v86, v85
	v_mul_f32_e32 v81, v86, v81
	v_mul_f32_e32 v82, v148, v82
	v_mul_f32_e32 v81, v149, v81
	v_cvt_pk_bf16_f32 v81, v82, v81
	v_add_u32_e32 v82, s1, v180
	ds_write_b128 v82, v[66:69]
	v_add_u32_e32 v66, s1, v181
	ds_write_b128 v66, v[70:73]
	v_add_u32_e32 v66, s1, v196
	ds_write_b128 v66, v[74:77] offset:32768
	v_add_u32_e32 v66, s1, v198
	ds_write_b128 v66, v[78:81] offset:32768
	s_waitcnt lgkmcnt(0)
	s_barrier
	s_cbranch_scc1 .LBB0_603
	v_mov_b32_e32 v200, v0
	s_branch .LBB0_469
